# speedup vs baseline: 1.0349x; 1.0036x over previous
_Z8k2_fusedPKDF16_PKDv8_DF16_PKfS5_S5_PfPiS6_:
	s_lshl_b32 s3, s2, 2
	s_ashr_i32 s16, s2, 4
	s_and_b32 s12, s3, 48
	s_lshl_b32 s2, s2, 4
	s_and_b32 s13, s2, 48
	s_add_i32 s2, s12, -2
	v_mul_u32_u24_e32 v1, 0x334, v0
	s_movk_i32 s15, 0xffec
	s_add_i32 s3, s13, -2
	v_lshrrev_b32_e32 v84, 2, v0
	v_mul_i32_i24_sdwa v2, v1, s15 dst_sel:DWORD dst_unused:UNUSED_PAD src0_sel:WORD_1 src1_sel:DWORD
	v_add_u32_sdwa v48, s2, v1 dst_sel:DWORD dst_unused:UNUSED_PAD src0_sel:DWORD src1_sel:WORD_1
	s_load_dwordx8 s[4:11], s[0:1], 0x0
	s_load_dwordx4 s[32:35], s[0:1], 0x20
	s_load_dwordx2 s[36:37], s[0:1], 0x38
	v_add3_u32 v49, s3, v84, v2
	v_max_i32_e32 v1, 0, v48
	s_lshl_b32 s14, s16, 12
	v_med3_i32 v2, v49, 0, 63
	v_lshlrev_b32_e32 v1, 6, v1
	v_or3_b32 v1, v1, v2, s14
	v_lshlrev_b32_e32 v2, 5, v1
	v_ashrrev_i32_e32 v3, 31, v2
	v_lshlrev_b32_e32 v85, 4, v0
	s_waitcnt lgkmcnt(0)
	v_lshl_add_u64 v[2:3], v[2:3], 1, s[4:5]
	v_and_b32_e32 v46, 48, v85
	v_mov_b32_e32 v47, 0
	v_or_b32_e32 v54, 0x200, v0
	v_lshl_add_u64 v[2:3], v[2:3], 0, v[46:47]
	v_mul_u32_u24_e32 v1, 0x334, v54
	global_load_dwordx4 v[18:21], v[2:3], off
	v_lshrrev_b32_e32 v86, 2, v54
	v_mul_i32_i24_sdwa v2, v1, s15 dst_sel:DWORD dst_unused:UNUSED_PAD src0_sel:WORD_1 src1_sel:DWORD
	v_add_u32_sdwa v50, s2, v1 dst_sel:DWORD dst_unused:UNUSED_PAD src0_sel:DWORD src1_sel:WORD_1
	v_add3_u32 v51, s3, v86, v2
	v_min_u32_e32 v1, 63, v50
	v_med3_i32 v2, v51, 0, 63
	v_lshlrev_b32_e32 v1, 6, v1
	v_or3_b32 v1, v1, v2, s14
	v_lshlrev_b32_e32 v2, 5, v1
	v_or_b32_e32 v58, 0x400, v0
	v_ashrrev_i32_e32 v3, 31, v2
	v_lshlrev_b32_e32 v87, 4, v54
	v_mul_u32_u24_e32 v1, 0x667, v58
	v_lshl_add_u64 v[2:3], v[2:3], 1, s[4:5]
	v_and_b32_e32 v4, 48, v87
	v_mov_b32_e32 v5, v47
	v_lshrrev_b32_e32 v1, 17, v1
	v_lshl_add_u64 v[2:3], v[2:3], 0, v[4:5]
	v_mul_i32_i24_e32 v4, 0xffffffec, v1
	v_add_u32_e32 v52, s2, v1
	v_lshrrev_b32_e32 v88, 2, v58
	v_add3_u32 v53, s3, v88, v4
	v_min_u32_e32 v1, 63, v52
	v_med3_i32 v4, v53, 0, 63
	v_lshlrev_b32_e32 v1, 6, v1
	v_or3_b32 v1, v1, v4, s14
	v_lshlrev_b32_e32 v4, 5, v1
	v_ashrrev_i32_e32 v5, 31, v4
	v_or_b32_e32 v89, 0x600, v0
	v_lshl_add_u64 v[4:5], v[4:5], 1, s[4:5]
	v_min_u32_e32 v1, 0x63f, v89
	v_lshl_add_u64 v[4:5], v[4:5], 0, v[46:47]
	global_load_dwordx4 v[22:25], v[2:3], off
	global_load_dwordx4 v[26:29], v[4:5], off
	v_lshrrev_b32_e32 v2, 2, v1
	v_add_u32_e32 v2, s3, v2
	s_add_i32 s15, s12, 17
	v_add_u32_e32 v55, 0xfffffe84, v2
	s_min_u32 s2, s15, 63
	v_min_u32_e32 v2, 63, v55
	v_lshl_or_b32 v2, s2, 6, v2
	v_or_b32_e32 v2, s14, v2
	v_lshlrev_b32_e32 v2, 5, v2
	v_ashrrev_i32_e32 v3, 31, v2
	v_lshlrev_b32_e32 v1, 4, v1
	v_lshl_add_u64 v[2:3], v[2:3], 1, s[4:5]
	v_and_b32_e32 v4, 48, v1
	v_mov_b32_e32 v5, v47
	v_min_u32_e32 v1, 0x47f, v58
	v_lshrrev_b32_e32 v164, 1, v0
	v_lshl_add_u64 v[2:3], v[2:3], 0, v[4:5]
	v_lshlrev_b32_e32 v90, 4, v1
	v_and_b32_e32 v162, 16, v164
	global_load_dwordx4 v[30:33], v[2:3], off
	global_load_dwordx4 v[34:37], v85, s[6:7]
	global_load_dwordx4 v[38:41], v87, s[6:7]
	global_load_dwordx4 v[42:45], v90, s[6:7]
	s_nop 0
	global_load_dwordx4 v[2:5], v162, s[8:9]
	global_load_dwordx4 v[6:9], v162, s[8:9] offset:32
	global_load_dwordx4 v[10:13], v162, s[8:9] offset:64
	global_load_dwordx4 v[14:17], v162, s[8:9] offset:96
	v_or_b32_e32 v48, v48, v49
	v_cmp_gt_u32_e32 vcc, 64, v48
	v_or_b32_e32 v48, v50, v51
	v_cmp_gt_u32_e64 s[2:3], 64, v48
	v_or_b32_e32 v48, v52, v53
	v_and_b32_e32 v1, 63, v0
	v_and_b32_e32 v165, 31, v0
	v_cmp_gt_u32_e64 s[4:5], 64, v48
	v_or_b32_e32 v48, s15, v55
	v_lshrrev_b32_e32 v163, 6, v0
	v_cmp_gt_u32_e64 s[6:7], 64, v48
	s_movk_i32 s8, 0x50
	s_waitcnt vmcnt(10)
	v_cndmask_b32_e32 v19, 0, v19, vcc
	v_cndmask_b32_e32 v18, 0, v18, vcc
	v_cndmask_b32_e32 v21, 0, v21, vcc
	v_cndmask_b32_e32 v20, 0, v20, vcc
	v_mad_u32_u24 v47, v84, s8, v46
	ds_write_b128 v47, v[18:21]
	s_waitcnt vmcnt(9)
	v_cndmask_b32_e64 v19, 0, v23, s[2:3]
	v_cndmask_b32_e64 v18, 0, v22, s[2:3]
	v_cndmask_b32_e64 v21, 0, v25, s[2:3]
	v_cndmask_b32_e64 v20, 0, v24, s[2:3]
	v_mad_u32_u24 v22, v86, s8, v46
	ds_write_b128 v22, v[18:21]
	s_waitcnt vmcnt(8)
	v_cndmask_b32_e64 v19, 0, v27, s[4:5]
	v_cndmask_b32_e64 v18, 0, v26, s[4:5]
	v_cndmask_b32_e64 v21, 0, v29, s[4:5]
	v_cndmask_b32_e64 v20, 0, v28, s[4:5]
	v_mad_u32_u24 v22, v88, s8, v46
	ds_write_b128 v22, v[18:21]
	v_lshrrev_b32_e32 v22, 2, v89
	s_waitcnt vmcnt(7)
	v_cndmask_b32_e64 v19, 0, v31, s[6:7]
	v_cndmask_b32_e64 v18, 0, v30, s[6:7]
	v_cndmask_b32_e64 v21, 0, v33, s[6:7]
	v_cndmask_b32_e64 v20, 0, v32, s[6:7]
	v_mad_u32_u24 v22, v22, s8, v46
	ds_write_b128 v22, v[18:21]
	s_waitcnt vmcnt(6)
	ds_write_b128 v85, v[34:37] offset:57920
	s_waitcnt vmcnt(5)
	ds_write_b128 v87, v[38:41] offset:57920
	s_waitcnt vmcnt(4)
	ds_write_b128 v90, v[42:45] offset:57920
	v_lshlrev_b32_e32 v18, 4, v1
	s_waitcnt lgkmcnt(0)
	s_barrier
	s_lshr_b32 s27, s12, 1
	s_lshr_b32 s26, s13, 1
	v_add_u32_e32 v48, s27, v163
	v_bfe_u32 v49, v0, 1, 3
	v_add_u32_e32 v49, s26, v49
	v_lshlrev_b32_e32 v48, 10, v48
	v_lshl_or_b32 v48, v49, 5, v48
	v_bfe_u32 v49, v0, 5, 1
	v_lshl_or_b32 v48, v49, 2, v48
	v_bfe_u32 v49, v0, 4, 1
	v_lshl_or_b32 v48, v49, 1, v48
	v_and_b32_e32 v49, 1, v0
	v_or_b32_e32 v48, v48, v49
	v_mul_u32_u24_e32 v196, 40, v48
	global_load_dwordx4 v[66:69], v196, s[10:11]
	global_load_dwordx4 v[50:53], v196, s[10:11] offset:16
	global_load_dwordx2 v[156:157], v196, s[10:11] offset:32
	global_load_dwordx4 v[70:73], v196, s[10:11] offset:320
	global_load_dwordx4 v[54:57], v196, s[10:11] offset:336
	global_load_dwordx2 v[154:155], v196, s[10:11] offset:352
	global_load_dwordx4 v[74:77], v196, s[10:11] offset:640
	global_load_dwordx4 v[58:61], v196, s[10:11] offset:656
	global_load_dwordx2 v[160:161], v196, s[10:11] offset:672
	global_load_dwordx4 v[78:81], v196, s[10:11] offset:960
	global_load_dwordx4 v[62:65], v196, s[10:11] offset:976
	global_load_dwordx2 v[158:159], v196, s[10:11] offset:992
	v_add_u32_e32 v19, 0xe240, v18
	ds_read_b128 v[150:153], v18 offset:57920
	ds_read_b128 v[146:149], v18 offset:58944
	ds_read_b128 v[142:145], v18 offset:59968
	ds_read_b128 v[138:141], v18 offset:60992
	ds_read_b128 v[134:137], v18 offset:62016
	ds_read_b128 v[130:133], v18 offset:63040
	ds_read_b128 v[126:129], v18 offset:64064
	ds_read_b128 v[122:125], v18 offset:65088
	ds_read_b128 v[118:121], v19 offset:8192
	ds_read_b128 v[114:117], v19 offset:9216
	ds_read_b128 v[110:113], v19 offset:10240
	ds_read_b128 v[106:109], v19 offset:11264
	ds_read_b128 v[102:105], v19 offset:12288
	ds_read_b128 v[98:101], v19 offset:13312
	ds_read_b128 v[94:97], v19 offset:14336
	ds_read_b128 v[90:93], v19 offset:15360
	ds_read_b128 v[86:89], v19 offset:16384
	ds_read_b128 v[82:85], v19 offset:17408
	v_lshl_or_b32 v166, v163, 5, v165
	v_mul_u32_u24_e32 v18, 0xe39, v166
	v_lshrrev_b32_e32 v168, 16, v18
	s_movk_i32 s4, 0xffee
	v_mad_i32_i24 v169, v168, s4, v166
	v_min_u32_e32 v19, 0x43, v166
	v_mad_u32_u24 v18, v168, 20, v169
	v_or_b32_e32 v165, 0x100, v19
	s_movk_i32 s2, 0xc0
	v_mul_lo_u32 v18, v18, s8
	v_mul_u32_u24_e32 v19, 0xe39, v165
	v_cmp_gt_u32_e32 vcc, s2, v0
	s_movk_i32 s2, 0xbf
	v_lshrrev_b32_e32 v167, 16, v19
	v_cmp_lt_u32_e64 s[2:3], s2, v0
	v_add_u32_e32 v171, v18, v162
	s_and_saveexec_b64 s[6:7], s[2:3]
	s_xor_b64 s[2:3], exec, s[6:7]
	s_cbranch_execz .LBB1_2
	ds_read_b128 v[34:37], v171
	ds_read_b128 v[38:41], v171 offset:32
	ds_read_b128 v[42:45], v171 offset:80
	ds_read_b128 v[46:49], v171 offset:112
	ds_read_b128 v[172:175], v171 offset:160
	ds_read_b128 v[176:179], v171 offset:192
	ds_read_b128 v[180:183], v171 offset:1600
	ds_read_b128 v[184:187], v171 offset:1632
	ds_read_b128 v[188:191], v171 offset:1680
	s_waitcnt vmcnt(12) lgkmcnt(8)
	v_mfma_f32_32x32x16_f16 v[18:33], v[150:153], v[34:37], v[2:17]
	s_waitcnt lgkmcnt(7)
	v_mfma_f32_32x32x16_f16 v[18:33], v[146:149], v[38:41], v[18:33]
	ds_read_b128 v[34:37], v171 offset:1712
	s_waitcnt lgkmcnt(7)
	v_mfma_f32_32x32x16_f16 v[18:33], v[142:145], v[42:45], v[18:33]
	ds_read_b128 v[38:41], v171 offset:1760
	s_waitcnt lgkmcnt(7)
	v_mfma_f32_32x32x16_f16 v[18:33], v[138:141], v[46:49], v[18:33]
	ds_read_b128 v[42:45], v171 offset:1792
	s_waitcnt lgkmcnt(7)
	v_mfma_f32_32x32x16_f16 v[18:33], v[134:137], v[172:175], v[18:33]
	ds_read_b128 v[46:49], v171 offset:3200
	s_waitcnt lgkmcnt(7)
	v_mfma_f32_32x32x16_f16 v[18:33], v[130:133], v[176:179], v[18:33]
	ds_read_b128 v[172:175], v171 offset:3232
	s_waitcnt lgkmcnt(7)
	v_mfma_f32_32x32x16_f16 v[18:33], v[126:129], v[180:183], v[18:33]
	ds_read_b128 v[176:179], v171 offset:3280
	s_waitcnt lgkmcnt(7)
	v_mfma_f32_32x32x16_f16 v[18:33], v[122:125], v[184:187], v[18:33]
	ds_read_b128 v[180:183], v171 offset:3312
	s_waitcnt lgkmcnt(7)
	v_mfma_f32_32x32x16_f16 v[18:33], v[118:121], v[188:191], v[18:33]
	ds_read_b128 v[184:187], v171 offset:3360
	s_waitcnt lgkmcnt(7)
	v_mfma_f32_32x32x16_f16 v[18:33], v[114:117], v[34:37], v[18:33]
	ds_read_b128 v[188:191], v171 offset:3392
	s_waitcnt lgkmcnt(7)
	v_mfma_f32_32x32x16_f16 v[18:33], v[110:113], v[38:41], v[18:33]
	s_waitcnt lgkmcnt(6)
	v_mfma_f32_32x32x16_f16 v[18:33], v[106:109], v[42:45], v[18:33]
	s_waitcnt lgkmcnt(5)
	v_mfma_f32_32x32x16_f16 v[18:33], v[102:105], v[46:49], v[18:33]
	s_waitcnt lgkmcnt(4)
	v_mfma_f32_32x32x16_f16 v[18:33], v[98:101], v[172:175], v[18:33]
	s_waitcnt lgkmcnt(3)
	v_mfma_f32_32x32x16_f16 v[18:33], v[94:97], v[176:179], v[18:33]
	s_waitcnt lgkmcnt(2)
	v_mfma_f32_32x32x16_f16 v[18:33], v[90:93], v[180:183], v[18:33]
	s_waitcnt lgkmcnt(1)
	v_mfma_f32_32x32x16_f16 v[18:33], v[86:89], v[184:187], v[18:33]
	s_waitcnt lgkmcnt(0)
	v_mfma_f32_32x32x16_f16 v[18:33], v[82:85], v[188:191], v[18:33]
	v_mov_b32_e32 v49, v17
	v_mov_b32_e32 v48, v16
	v_mov_b32_e32 v47, v15
	v_mov_b32_e32 v46, v14
	v_mov_b32_e32 v45, v13
	v_mov_b32_e32 v44, v12
	v_mov_b32_e32 v43, v11
	v_mov_b32_e32 v42, v10
	v_mov_b32_e32 v41, v9
	v_mov_b32_e32 v40, v8
	v_mov_b32_e32 v39, v7
	v_mov_b32_e32 v38, v6
	v_mov_b32_e32 v37, v5
	v_mov_b32_e32 v36, v4
	v_mov_b32_e32 v35, v3
	v_mov_b32_e32 v34, v2
